# speedup vs baseline: 1.0104x; 1.0040x over previous
.LBB3_2:
	v_lshl_add_u64 v[40:41], v[4:5], 0, s[0:1]
	global_load_dwordx4 v[8:11], v[40:41], off nt
	global_load_dwordx4 v[12:15], v[40:41], off offset:400 nt
	global_load_dwordx4 v[16:19], v[40:41], off offset:800 nt
	global_load_dwordx4 v[20:23], v[40:41], off offset:1200 nt
	global_load_dwordx4 v[24:27], v[40:41], off offset:1600 nt
	global_load_dwordx4 v[28:31], v[40:41], off offset:2000 nt
	global_load_dwordx4 v[32:35], v[40:41], off offset:2400 nt
	global_load_dwordx4 v[36:39], v[40:41], off offset:2800 nt
	v_add_co_u32_e32 v56, vcc, s5, v40
	s_nop 1
	v_addc_co_u32_e32 v57, vcc, 0, v41, vcc
	v_add_co_u32_e32 v68, vcc, s6, v40
	s_nop 1
	v_addc_co_u32_e32 v69, vcc, 0, v41, vcc
	global_load_dwordx4 v[40:43], v[56:57], off offset:2304 nt
	global_load_dwordx4 v[44:47], v[56:57], off offset:2704 nt
	global_load_dwordx4 v[48:51], v[56:57], off offset:3104 nt
	global_load_dwordx4 v[52:55], v[56:57], off offset:3504 nt
	global_load_dwordx4 v[56:59], v[56:57], off offset:3904 nt
	global_load_dwordx4 v[60:63], v[68:69], off offset:208 nt
	global_load_dwordx4 v[64:67], v[68:69], off offset:608 nt
	global_load_dwordx4 v[68:71], v[68:69], off offset:1008 nt
	s_and_b32 s2, s7, 0x4000
	s_sub_i32 s12, s4, 32
	s_and_b32 s12, s12, 64
	s_add_u32 s12, s12, s2
	s_and_b32 s13, s4, 0x60
	s_add_u32 s13, s13, s2
	s_waitcnt vmcnt(16)
	v_lshrrev_b32_e32 v90, 7, v89
	v_lshlrev_b32_e32 v90, 19, v90
	v_lshlrev_b32_e32 v91, 7, v89
	v_and_b32_e32 v91, 0x3f80, v91
	v_add3_u32 v90, v90, v91, v88
	v_add_u32_e32 v72, s12, v90
	v_add_u32_e32 v76, s13, v90
	global_load_dwordx4 v[72:75], v72, s[14:15]
	global_load_dwordx4 v[76:79], v76, s[14:15]
	s_add_i32 s4, s4, 64
	s_add_u32 s0, s0, 0x3200
	s_addc_u32 s1, s1, 0
	s_addk_i32 s7, 0x2000
	s_cmpk_eq_u32 s0, 0xc800
	s_waitcnt vmcnt(16)
	v_cvt_pk_f16_f32 v80, v8, v12
	s_waitcnt vmcnt(14)
	v_cvt_pk_f16_f32 v81, v16, v20
	v_cvt_pk_f16_f32 v19, v19, v23
	s_waitcnt vmcnt(12)
	v_cvt_pk_f16_f32 v82, v24, v28
	v_cvt_pk_f16_f32 v84, v25, v29
	s_waitcnt vmcnt(10)
	v_cvt_pk_f16_f32 v83, v32, v36
	v_cvt_pk_f16_f32 v85, v33, v37
	v_cvt_pk_f16_f32 v87, v34, v38
	v_cvt_pk_f16_f32 v86, v26, v30
	v_cvt_pk_f16_f32 v20, v27, v31
	s_waitcnt vmcnt(1)
	v_mfma_f32_32x32x16_f16 a[0:15], v[80:83], v[72:75], a[0:15]
	v_cvt_pk_f16_f32 v83, v17, v21
	v_cvt_pk_f16_f32 v82, v9, v13
	v_cvt_pk_f16_f32 v9, v48, v52
	v_cvt_pk_f16_f32 v8, v40, v44
	v_cvt_pk_f16_f32 v21, v35, v39
	v_cvt_pk_f16_f32 v13, v65, v69
	v_cvt_pk_f16_f32 v12, v57, v61
	v_mfma_f32_32x32x16_f16 a[16:31], v[82:85], v[72:75], a[16:31]
	v_cvt_pk_f16_f32 v85, v18, v22
	v_cvt_pk_f16_f32 v84, v10, v14
	v_cvt_pk_f16_f32 v18, v11, v15
	v_cvt_pk_f16_f32 v11, v64, v68
	v_cvt_pk_f16_f32 v10, v56, v60
	v_cvt_pk_f16_f32 v15, v66, v70
	v_cvt_pk_f16_f32 v14, v58, v62
	s_waitcnt vmcnt(0)
	v_mfma_f32_32x32x16_f16 a[0:15], v[8:11], v[76:79], a[0:15]
	v_cvt_pk_f16_f32 v11, v49, v53
	v_cvt_pk_f16_f32 v10, v41, v45
	v_cvt_pk_f16_f32 v9, v51, v55
	v_cvt_pk_f16_f32 v8, v43, v47
	v_mfma_f32_32x32x16_f16 a[32:47], v[84:87], v[72:75], a[32:47]
	v_mfma_f32_32x32x16_f16 a[48:63], v[18:21], v[72:75], a[48:63]
	v_mfma_f32_32x32x16_f16 a[16:31], v[10:13], v[76:79], a[16:31]
	v_cvt_pk_f16_f32 v13, v50, v54
	v_cvt_pk_f16_f32 v12, v42, v46
	v_cvt_pk_f16_f32 v11, v67, v71
	v_cvt_pk_f16_f32 v10, v59, v63
	v_mfma_f32_32x32x16_f16 a[32:47], v[12:15], v[76:79], a[32:47]
	s_nop 0
	v_mfma_f32_32x32x16_f16 a[48:63], v[8:11], v[76:79], a[48:63]
	s_cbranch_scc0 .LBB3_2
	v_mul_u32_u24_e32 v2, 0x190, v6
	s_movk_i32 s0, 0x3200
	v_mad_u32_u24 v2, v7, s0, v2
	v_lshl_add_u32 v3, v1, 6, v2
	s_nop 6
	v_accvgpr_mov_b32 a63, a16
	v_accvgpr_mov_b32 a14, a1
	v_accvgpr_mov_b32 a15, a17
	v_accvgpr_mov_b32 a16, a33
	v_accvgpr_mov_b32 a17, a49
	v_accvgpr_mov_b32 a65, a48
	ds_write_b128 v3, a[14:17] offset:16
	v_accvgpr_mov_b32 a17, a50
	v_accvgpr_mov_b32 a48, a3
	v_accvgpr_mov_b32 a49, a19
	v_accvgpr_mov_b32 a50, a35
	v_accvgpr_mov_b32 a62, a0
	v_accvgpr_mov_b32 a14, a2
	ds_write_b128 v3, a[48:51] offset:48
	v_accvgpr_mov_b32 a0, a4
	v_accvgpr_mov_b32 a1, a20
	v_accvgpr_mov_b32 a2, a36
	v_accvgpr_mov_b32 a3, a52
	v_accvgpr_mov_b32 a50, a5
	v_accvgpr_mov_b32 a51, a21
	v_accvgpr_mov_b32 a52, a37
	ds_write_b128 v3, a[0:3] offset:128
	ds_write_b128 v3, a[50:53] offset:144
	v_accvgpr_mov_b32 a0, a6
	v_accvgpr_mov_b32 a1, a22
	v_accvgpr_mov_b32 a2, a38
	v_accvgpr_mov_b32 a3, a54
	v_accvgpr_mov_b32 a52, a7
	v_accvgpr_mov_b32 a53, a23
	v_accvgpr_mov_b32 a54, a39
	ds_write_b128 v3, a[0:3] offset:160
	ds_write_b128 v3, a[52:55] offset:176
	v_accvgpr_mov_b32 a0, a8
	v_accvgpr_mov_b32 a1, a24
	v_accvgpr_mov_b32 a2, a40
	v_accvgpr_mov_b32 a3, a56
	v_accvgpr_mov_b32 a54, a9
	v_accvgpr_mov_b32 a55, a25
	v_accvgpr_mov_b32 a56, a41
	v_accvgpr_mov_b32 a64, a32
	v_accvgpr_mov_b32 a15, a18
	v_accvgpr_mov_b32 a16, a34
	ds_write_b128 v3, a[0:3] offset:256
	ds_write_b128 v3, a[54:57] offset:272
	v_accvgpr_mov_b32 a0, a10
	v_accvgpr_mov_b32 a1, a26
	v_accvgpr_mov_b32 a2, a42
	v_accvgpr_mov_b32 a3, a58
	v_accvgpr_mov_b32 a56, a11
	v_accvgpr_mov_b32 a57, a27
	v_accvgpr_mov_b32 a58, a43
	v_cmp_eq_u32_e32 vcc, 0, v1
	ds_write_b128 v3, a[62:65]
	ds_write_b128 v3, a[14:17] offset:32
	ds_write_b128 v3, a[0:3] offset:288
	ds_write_b128 v3, a[56:59] offset:304
	s_and_saveexec_b64 s[0:1], vcc
	v_accvgpr_mov_b32 a13, a28
	v_accvgpr_mov_b32 a14, a44
	v_accvgpr_mov_b32 a15, a60
	ds_write_b128 v2, a[12:15] offset:384
	s_or_b64 exec, exec, s[0:1]
	s_movk_i32 s0, 0x320
	v_cmp_gt_u32_e32 vcc, s0, v0
	s_waitcnt lgkmcnt(0)
	s_barrier
	s_and_saveexec_b64 s[0:1], vcc
	s_cbranch_execz .LBB3_8
	s_mul_i32 s1, s8, 0xc800
	s_mulk_i32 s9, 0x3200
	s_mul_hi_u32 s0, s8, 0xc800
	s_add_u32 s1, s1, s9
	s_addc_u32 s2, s0, 0
	s_add_u32 s0, s10, s1
	v_or_b32_e32 v4, 0xffffff00, v0
	v_lshlrev_b32_e32 v0, 4, v0
	v_mov_b32_e32 v1, 0
	s_addc_u32 s1, s11, s2
	v_lshl_add_u64 v[2:3], s[0:1], 0, v[0:1]
	s_mov_b64 s[0:1], 0
	s_mov_b32 s2, 0x3d000000
	s_mov_b64 s[4:5], 0x1000
	s_movk_i32 s3, 0x21f

.LBB9_6:
	s_or_b64 exec, exec, s[18:19]
	s_lshl_b32 s23, s3, 4
	s_waitcnt lgkmcnt(0)
	s_cmp_ge_i32 s23, s2
	s_mov_b64 s[18:19], -1
	s_cbranch_scc1 .LBB9_3
	v_or_b32_e32 v49, s23, v44
	v_mad_i64_i32 v[50:51], s[18:19], v49, s22, 0
	v_lshl_add_u64 v[58:59], v[50:51], 2, s[20:21]
	v_lshl_add_u64 v[60:61], v[4:5], 2, v[58:59]
	v_lshl_add_u64 v[62:63], v[14:15], 2, v[58:59]
	global_load_dwordx4 v[50:53], v[60:61], off
	global_load_dwordx4 v[54:57], v[62:63], off
	global_load_dword v66, v[6:7], off
	global_load_dword v70, v[8:9], off
	global_load_dword v71, v[10:11], off
	global_load_dword v72, v[12:13], off
	global_load_dword v73, v[16:17], off
	global_load_dword v74, v[18:19], off
	global_load_dword v75, v[20:21], off
	global_load_dword v76, v[22:23], off
	v_lshl_add_u64 v[60:61], v[24:25], 2, v[58:59]
	v_lshl_add_u64 v[62:63], v[34:35], 2, v[58:59]
	global_load_dwordx4 v[58:61], v[60:61], off
	global_load_dwordx4 v[62:65], v[62:63], off
	global_load_dword v77, v[26:27], off
	global_load_dword v78, v[28:29], off
	global_load_dword v79, v[30:31], off
	global_load_dword v80, v[32:33], off
	global_load_dword v81, v[36:37], off
	global_load_dword v82, v[38:39], off
	global_load_dword v83, v[40:41], off
	global_load_dword v84, v[42:43], off
	v_or_b32_e32 v49, s23, v45
	s_waitcnt vmcnt(19)
	v_cndmask_b32_e64 v50, 0, v50, s[6:7]
	s_waitcnt vmcnt(18)
	v_cndmask_b32_e64 v54, 0, v54, s[8:9]
	v_cmp_le_i32_e32 vcc, s2, v49
	s_or_b64 s[18:19], s[16:17], vcc
	s_nor_b64 s[24:25], s[18:19], s[14:15]
	s_waitcnt vmcnt(17)
	v_mfma_f32_16x16x4_f32 v[66:69], v50, v66, 0
	v_cndmask_b32_e64 v50, 0, v51, s[6:7]
	s_waitcnt vmcnt(16)
	s_nop 0
	v_mfma_f32_16x16x4_f32 v[66:69], v50, v70, v[66:69]
	v_cndmask_b32_e64 v50, 0, v52, s[6:7]
	s_waitcnt vmcnt(15)
	s_nop 0
	v_mfma_f32_16x16x4_f32 v[66:69], v50, v71, v[66:69]
	v_cndmask_b32_e64 v50, 0, v53, s[6:7]
	s_waitcnt vmcnt(14)
	s_nop 0
	v_mfma_f32_16x16x4_f32 v[50:53], v50, v72, v[66:69]
	s_waitcnt vmcnt(13)
	v_mfma_f32_16x16x4_f32 v[50:53], v54, v73, v[50:53]
	v_cndmask_b32_e64 v54, 0, v55, s[8:9]
	s_waitcnt vmcnt(12)
	s_nop 0
	v_mfma_f32_16x16x4_f32 v[50:53], v54, v74, v[50:53]
	v_cndmask_b32_e64 v54, 0, v56, s[8:9]
	s_waitcnt vmcnt(11)
	s_nop 0
	v_mfma_f32_16x16x4_f32 v[50:53], v54, v75, v[50:53]
	v_cndmask_b32_e64 v54, 0, v57, s[8:9]
	s_waitcnt vmcnt(10)
	s_nop 0
	v_mfma_f32_16x16x4_f32 v[50:53], v54, v76, v[50:53]
	s_waitcnt vmcnt(9)
	v_cndmask_b32_e64 v54, 0, v58, s[10:11]
	s_waitcnt vmcnt(7)
	s_nop 0
	v_mfma_f32_16x16x4_f32 v[50:53], v54, v77, v[50:53]
	v_cndmask_b32_e64 v54, 0, v59, s[10:11]
	s_waitcnt vmcnt(6)
	s_nop 0
	v_mfma_f32_16x16x4_f32 v[50:53], v54, v78, v[50:53]
	v_cndmask_b32_e64 v54, 0, v60, s[10:11]
	s_waitcnt vmcnt(5)
	s_nop 0
	v_mfma_f32_16x16x4_f32 v[50:53], v54, v79, v[50:53]
	v_cndmask_b32_e64 v54, 0, v61, s[10:11]
	s_waitcnt vmcnt(4)
	s_nop 0
	v_mfma_f32_16x16x4_f32 v[50:53], v54, v80, v[50:53]
	v_cndmask_b32_e64 v54, 0, v62, s[12:13]
	s_waitcnt vmcnt(3)
	s_nop 0
	v_mfma_f32_16x16x4_f32 v[50:53], v54, v81, v[50:53]
	v_cndmask_b32_e64 v54, 0, v63, s[12:13]
	s_waitcnt vmcnt(2)
	s_nop 0
	v_mfma_f32_16x16x4_f32 v[50:53], v54, v82, v[50:53]
	v_cndmask_b32_e64 v54, 0, v64, s[12:13]
	s_waitcnt vmcnt(1)
	s_nop 0
	v_mfma_f32_16x16x4_f32 v[50:53], v54, v83, v[50:53]
	v_cndmask_b32_e64 v54, 0, v65, s[12:13]
	s_waitcnt vmcnt(0)
	s_nop 0
	v_mfma_f32_16x16x4_f32 v[50:53], v54, v84, v[50:53]
	s_nop 9
	ds_write2st64_b32 v46, v50, v51 offset1:1
	ds_write2st64_b32 v46, v52, v53 offset0:2 offset1:3
	s_waitcnt lgkmcnt(0)
	s_barrier
	s_and_saveexec_b64 s[18:19], s[24:25]
	s_cbranch_execz .LBB9_2
	ds_read2st64_b32 v[50:51], v47 offset1:4
	ds_read2st64_b32 v[52:53], v47 offset0:8 offset1:12
	ds_read2st64_b32 v[54:55], v47 offset0:16 offset1:20
	ds_read2st64_b32 v[56:57], v47 offset0:24 offset1:28
	ds_read2st64_b32 v[58:59], v47 offset0:32 offset1:36
	s_waitcnt lgkmcnt(4)
	v_add_f32_e32 v50, 0, v50
	v_add_f32_e32 v50, v50, v51
	s_waitcnt lgkmcnt(3)
	v_add_f32_e32 v50, v50, v52
	v_add_f32_e32 v50, v50, v53
	s_waitcnt lgkmcnt(2)
	v_add_f32_e32 v50, v50, v54
	v_add_f32_e32 v50, v50, v55
	s_waitcnt lgkmcnt(1)
	v_add_f32_e32 v50, v50, v56
	v_add_f32_e32 v52, v50, v57
	ds_read2st64_b32 v[50:51], v47 offset0:40 offset1:44
	s_waitcnt lgkmcnt(1)
	v_add_f32_e32 v54, v52, v58
	ds_read2st64_b32 v[52:53], v47 offset0:48 offset1:52
	v_add_f32_e32 v56, v54, v59
	ds_read2st64_b32 v[54:55], v47 offset0:56 offset1:60
	s_waitcnt lgkmcnt(2)
	v_add_f32_e32 v50, v56, v50
	v_add_f32_e32 v50, v50, v51
	s_waitcnt lgkmcnt(1)
	v_add_f32_e32 v50, v50, v52
	v_add_f32_e32 v50, v50, v53
	s_waitcnt lgkmcnt(0)
	v_add_f32_e32 v50, v50, v54
	v_add_f32_e32 v50, v50, v55
	v_add_f32_e32 v48, v48, v50
	v_max_f32_e32 v50, 0, v48
	v_mad_i64_i32 v[48:49], s[24:25], v49, s28, 0
	v_lshl_add_u64 v[48:49], v[48:49], 2, v[0:1]
	global_store_dword v[48:49], v50, off
	s_branch .LBB9_2
